# accumulator zeroing via v_mov_b64 in 16 GEMM phases (incl. MoE gate/up)
# baseline (speedup 1.0000x reference)
.LBB0_235:
	s_ashr_i32 s15, s14, 31
	s_lshl_b64 s[16:17], s[14:15], 19
	s_add_u32 s16, s38, s16
	s_addc_u32 s17, s39, s17
	s_and_b64 s[18:19], s[4:5], exec
	s_cselect_b32 s15, s17, s41
	s_cselect_b32 s56, s16, s40
	s_ashr_i32 s13, s12, 31
	s_lshl_b64 s[18:19], s[12:13], 19
	s_add_u32 s18, s3, s18
	s_addc_u32 s19, s30, s19
	s_and_b64 s[28:29], s[4:5], exec
	s_cselect_b32 s13, s19, s23
	s_cselect_b32 s57, s18, s22
	s_add_u32 s58, s22, 0x10000
	s_addc_u32 s59, s23, 0
	s_add_u32 s22, s40, 0x40080
	v_mov_b32_e32 v2, 0
	s_addc_u32 s23, s41, 0
	s_mov_b32 s28, -2
	v_mov_b32_e32 v3, 0
	v_mov_b64_e32 v[4:5], 0
	v_mov_b64_e32 v[6:7], 0
	v_mov_b64_e32 v[8:9], 0
	v_mov_b64_e32 v[10:11], 0
	v_mov_b64_e32 v[12:13], 0
	v_mov_b64_e32 v[14:15], 0
	v_mov_b64_e32 v[16:17], 0
	v_mov_b64_e32 v[18:19], 0
	v_mov_b64_e32 v[20:21], 0
	v_mov_b64_e32 v[22:23], 0
	v_mov_b64_e32 v[24:25], 0
	v_mov_b64_e32 v[26:27], 0
	v_mov_b64_e32 v[28:29], 0
	v_mov_b64_e32 v[30:31], 0
	v_mov_b64_e32 v[32:33], 0
	v_mov_b64_e32 v[34:35], 0
	v_mov_b64_e32 v[36:37], 0
	v_mov_b64_e32 v[38:39], 0
	v_mov_b64_e32 v[40:41], 0
	v_mov_b64_e32 v[42:43], 0
	v_mov_b64_e32 v[44:45], 0
	v_mov_b64_e32 v[46:47], 0
	v_mov_b64_e32 v[48:49], 0
	v_mov_b64_e32 v[50:51], 0
	v_mov_b64_e32 v[52:53], 0
	v_mov_b64_e32 v[54:55], 0
	v_mov_b64_e32 v[56:57], 0
	v_mov_b64_e32 v[58:59], 0
	v_mov_b64_e32 v[60:61], 0
	v_mov_b64_e32 v[62:63], 0
	v_mov_b64_e32 v[64:65], 0
	v_mov_b64_e32 v[66:67], 0
	v_mov_b64_e32 v[68:69], 0
	v_mov_b64_e32 v[70:71], 0
	v_mov_b64_e32 v[72:73], 0
	v_mov_b64_e32 v[74:75], 0
	v_mov_b64_e32 v[76:77], 0
	v_mov_b64_e32 v[78:79], 0
	v_mov_b64_e32 v[80:81], 0
	v_mov_b64_e32 v[82:83], 0
	v_mov_b64_e32 v[84:85], 0
	v_mov_b64_e32 v[86:87], 0
	v_mov_b64_e32 v[88:89], 0
	v_mov_b64_e32 v[90:91], 0
	v_mov_b64_e32 v[92:93], 0
	v_mov_b64_e32 v[94:95], 0
	v_mov_b64_e32 v[96:97], 0
	v_mov_b64_e32 v[98:99], 0
	v_mov_b64_e32 v[100:101], 0
	v_mov_b64_e32 v[102:103], 0
	v_mov_b64_e32 v[104:105], 0
	v_mov_b64_e32 v[106:107], 0
	v_mov_b64_e32 v[108:109], 0
	v_mov_b64_e32 v[110:111], 0
	v_mov_b64_e32 v[112:113], 0
	v_mov_b64_e32 v[114:115], 0
	v_mov_b64_e32 v[116:117], 0
	v_mov_b64_e32 v[118:119], 0
	v_mov_b64_e32 v[120:121], 0
	v_mov_b64_e32 v[122:123], 0
	v_mov_b64_e32 v[124:125], 0
	v_mov_b64_e32 v[126:127], 0
	v_mov_b64_e32 v[128:129], 0

.LBB0_608:
	s_cmp_lt_i32 s42, 0
	s_cselect_b32 s33, 32, 4
	s_add_i32 s43, s33, -2
	s_add_u32 s45, s56, 0x10000
	s_addc_u32 s47, s57, 0
	s_add_u32 s56, s58, 0x80080
	v_mov_b32_e32 v2, 0
	s_mov_b32 s28, 0
	s_addc_u32 s57, s59, 0
	v_mov_b32_e32 v3, 0
	v_mov_b64_e32 v[4:5], 0
	v_mov_b64_e32 v[6:7], 0
	v_mov_b64_e32 v[8:9], 0
	v_mov_b64_e32 v[10:11], 0
	v_mov_b64_e32 v[12:13], 0
	v_mov_b64_e32 v[14:15], 0
	v_mov_b64_e32 v[16:17], 0
	v_mov_b64_e32 v[18:19], 0
	v_mov_b64_e32 v[20:21], 0
	v_mov_b64_e32 v[22:23], 0
	v_mov_b64_e32 v[24:25], 0
	v_mov_b64_e32 v[26:27], 0
	v_mov_b64_e32 v[28:29], 0
	v_mov_b64_e32 v[30:31], 0
	v_mov_b64_e32 v[32:33], 0
	v_mov_b64_e32 v[34:35], 0
	v_mov_b64_e32 v[36:37], 0
	v_mov_b64_e32 v[38:39], 0
	v_mov_b64_e32 v[40:41], 0
	v_mov_b64_e32 v[42:43], 0
	v_mov_b64_e32 v[44:45], 0
	v_mov_b64_e32 v[46:47], 0
	v_mov_b64_e32 v[48:49], 0
	v_mov_b64_e32 v[50:51], 0
	v_mov_b64_e32 v[52:53], 0
	v_mov_b64_e32 v[54:55], 0
	v_mov_b64_e32 v[56:57], 0
	v_mov_b64_e32 v[58:59], 0
	v_mov_b64_e32 v[60:61], 0
	v_mov_b64_e32 v[62:63], 0
	v_mov_b64_e32 v[64:65], 0
	v_mov_b64_e32 v[66:67], 0
	v_mov_b64_e32 v[68:69], 0
	v_mov_b64_e32 v[70:71], 0
	v_mov_b64_e32 v[72:73], 0
	v_mov_b64_e32 v[74:75], 0
	v_mov_b64_e32 v[76:77], 0
	v_mov_b64_e32 v[78:79], 0
	v_mov_b64_e32 v[80:81], 0
	v_mov_b64_e32 v[82:83], 0
	v_mov_b64_e32 v[84:85], 0
	v_mov_b64_e32 v[86:87], 0
	v_mov_b64_e32 v[88:89], 0
	v_mov_b64_e32 v[90:91], 0
	v_mov_b64_e32 v[92:93], 0
	v_mov_b64_e32 v[94:95], 0
	v_mov_b64_e32 v[96:97], 0
	v_mov_b64_e32 v[98:99], 0
	v_mov_b64_e32 v[100:101], 0
	v_mov_b64_e32 v[102:103], 0
	v_mov_b64_e32 v[104:105], 0
	v_mov_b64_e32 v[106:107], 0
	v_mov_b64_e32 v[108:109], 0
	v_mov_b64_e32 v[110:111], 0
	v_mov_b64_e32 v[112:113], 0
	v_mov_b64_e32 v[114:115], 0
	v_mov_b64_e32 v[116:117], 0
	v_mov_b64_e32 v[118:119], 0
	v_mov_b64_e32 v[120:121], 0
	v_mov_b64_e32 v[122:123], 0
	v_mov_b64_e32 v[124:125], 0
	v_mov_b64_e32 v[126:127], 0
	v_mov_b64_e32 v[128:129], 0

.LBB0_738:
	s_ashr_i32 s17, s16, 31
	s_lshl_b64 s[18:19], s[16:17], 19
	s_add_u32 s18, s38, s18
	s_addc_u32 s19, s39, s19
	s_and_b64 s[20:21], s[4:5], exec
	s_cselect_b32 s17, s19, s47
	s_cselect_b32 s43, s18, s46
	s_ashr_i32 s15, s14, 31
	s_lshl_b64 s[20:21], s[14:15], 19
	s_add_u32 s20, s3, s20
	s_addc_u32 s21, s30, s21
	s_and_b64 s[28:29], s[4:5], exec
	s_cselect_b32 s15, s21, s45
	s_cselect_b32 s63, s20, s44
	s_add_u32 s64, s44, 0x10000
	s_addc_u32 s65, s45, 0
	s_add_u32 s44, s46, 0x40080
	v_mov_b32_e32 v2, 0
	s_addc_u32 s45, s47, 0
	s_mov_b32 s28, -2
	v_mov_b32_e32 v3, 0
	v_mov_b64_e32 v[4:5], 0
	v_mov_b64_e32 v[6:7], 0
	v_mov_b64_e32 v[8:9], 0
	v_mov_b64_e32 v[10:11], 0
	v_mov_b64_e32 v[12:13], 0
	v_mov_b64_e32 v[14:15], 0
	v_mov_b64_e32 v[16:17], 0
	v_mov_b64_e32 v[18:19], 0
	v_mov_b64_e32 v[20:21], 0
	v_mov_b64_e32 v[22:23], 0
	v_mov_b64_e32 v[24:25], 0
	v_mov_b64_e32 v[26:27], 0
	v_mov_b64_e32 v[28:29], 0
	v_mov_b64_e32 v[30:31], 0
	v_mov_b64_e32 v[32:33], 0
	v_mov_b64_e32 v[34:35], 0
	v_mov_b64_e32 v[36:37], 0
	v_mov_b64_e32 v[38:39], 0
	v_mov_b64_e32 v[40:41], 0
	v_mov_b64_e32 v[42:43], 0
	v_mov_b64_e32 v[44:45], 0
	v_mov_b64_e32 v[46:47], 0
	v_mov_b64_e32 v[48:49], 0
	v_mov_b64_e32 v[50:51], 0
	v_mov_b64_e32 v[52:53], 0
	v_mov_b64_e32 v[54:55], 0
	v_mov_b64_e32 v[56:57], 0
	v_mov_b64_e32 v[58:59], 0
	v_mov_b64_e32 v[60:61], 0
	v_mov_b64_e32 v[62:63], 0
	v_mov_b64_e32 v[64:65], 0
	v_mov_b64_e32 v[66:67], 0
	v_mov_b64_e32 v[68:69], 0
	v_mov_b64_e32 v[70:71], 0
	v_mov_b64_e32 v[72:73], 0
	v_mov_b64_e32 v[74:75], 0
	v_mov_b64_e32 v[76:77], 0
	v_mov_b64_e32 v[78:79], 0
	v_mov_b64_e32 v[80:81], 0
	v_mov_b64_e32 v[82:83], 0
	v_mov_b64_e32 v[84:85], 0
	v_mov_b64_e32 v[86:87], 0
	v_mov_b64_e32 v[88:89], 0
	v_mov_b64_e32 v[90:91], 0
	v_mov_b64_e32 v[92:93], 0
	v_mov_b64_e32 v[94:95], 0
	v_mov_b64_e32 v[96:97], 0
	v_mov_b64_e32 v[98:99], 0
	v_mov_b64_e32 v[100:101], 0
	v_mov_b64_e32 v[102:103], 0
	v_mov_b64_e32 v[104:105], 0
	v_mov_b64_e32 v[106:107], 0
	v_mov_b64_e32 v[108:109], 0
	v_mov_b64_e32 v[110:111], 0
	v_mov_b64_e32 v[112:113], 0
	v_mov_b64_e32 v[114:115], 0
	v_mov_b64_e32 v[116:117], 0
	v_mov_b64_e32 v[118:119], 0
	v_mov_b64_e32 v[120:121], 0
	v_mov_b64_e32 v[122:123], 0
	v_mov_b64_e32 v[124:125], 0
	v_mov_b64_e32 v[126:127], 0
	v_mov_b64_e32 v[128:129], 0

.LBB0_823:
	s_cmp_lt_i32 s22, 0
	s_cselect_b32 s23, 44, 4
	s_add_i32 s73, s23, -2
	s_add_u32 s46, s46, 0xc000
	s_addc_u32 s47, s47, 0
	s_add_u32 s76, s48, 0x10000
	v_mov_b32_e32 v2, 0
	s_mov_b32 s28, 0
	s_addc_u32 s77, s49, 0
	v_mov_b32_e32 v3, 0
	v_mov_b64_e32 v[4:5], 0
	v_mov_b64_e32 v[6:7], 0
	v_mov_b64_e32 v[8:9], 0
	v_mov_b64_e32 v[10:11], 0
	v_mov_b64_e32 v[12:13], 0
	v_mov_b64_e32 v[14:15], 0
	v_mov_b64_e32 v[16:17], 0
	v_mov_b64_e32 v[18:19], 0
	v_mov_b64_e32 v[20:21], 0
	v_mov_b64_e32 v[22:23], 0
	v_mov_b64_e32 v[24:25], 0
	v_mov_b64_e32 v[26:27], 0
	v_mov_b64_e32 v[28:29], 0
	v_mov_b64_e32 v[30:31], 0
	v_mov_b64_e32 v[32:33], 0
	v_mov_b64_e32 v[34:35], 0
	v_mov_b64_e32 v[36:37], 0
	v_mov_b64_e32 v[38:39], 0
	v_mov_b64_e32 v[40:41], 0
	v_mov_b64_e32 v[42:43], 0
	v_mov_b64_e32 v[44:45], 0
	v_mov_b64_e32 v[46:47], 0
	v_mov_b64_e32 v[48:49], 0
	v_mov_b64_e32 v[50:51], 0
	v_mov_b64_e32 v[52:53], 0
	v_mov_b64_e32 v[54:55], 0
	v_mov_b64_e32 v[56:57], 0
	v_mov_b64_e32 v[58:59], 0
	v_mov_b64_e32 v[60:61], 0
	v_mov_b64_e32 v[62:63], 0
	v_mov_b64_e32 v[64:65], 0
	v_mov_b64_e32 v[66:67], 0
	v_mov_b64_e32 v[68:69], 0
	v_mov_b64_e32 v[70:71], 0
	v_mov_b64_e32 v[72:73], 0
	v_mov_b64_e32 v[74:75], 0
	v_mov_b64_e32 v[76:77], 0
	v_mov_b64_e32 v[78:79], 0
	v_mov_b64_e32 v[80:81], 0
	v_mov_b64_e32 v[82:83], 0
	v_mov_b64_e32 v[84:85], 0
	v_mov_b64_e32 v[86:87], 0
	v_mov_b64_e32 v[88:89], 0
	v_mov_b64_e32 v[90:91], 0
	v_mov_b64_e32 v[92:93], 0
	v_mov_b64_e32 v[94:95], 0
	v_mov_b64_e32 v[96:97], 0
	v_mov_b64_e32 v[98:99], 0
	v_mov_b64_e32 v[100:101], 0
	v_mov_b64_e32 v[102:103], 0
	v_mov_b64_e32 v[104:105], 0
	v_mov_b64_e32 v[106:107], 0
	v_mov_b64_e32 v[108:109], 0
	v_mov_b64_e32 v[110:111], 0
	v_mov_b64_e32 v[112:113], 0
	v_mov_b64_e32 v[114:115], 0
	v_mov_b64_e32 v[116:117], 0
	v_mov_b64_e32 v[118:119], 0
	v_mov_b64_e32 v[120:121], 0
	v_mov_b64_e32 v[122:123], 0
	v_mov_b64_e32 v[124:125], 0
	v_mov_b64_e32 v[126:127], 0
	v_mov_b64_e32 v[128:129], 0

.LBB0_957:
	s_ashr_i32 s19, s18, 31
	s_lshl_b64 s[20:21], s[18:19], 19
	s_add_u32 s20, s38, s20
	s_addc_u32 s21, s39, s21
	s_and_b64 s[22:23], s[4:5], exec
	s_cselect_b32 s19, s21, s45
	s_cselect_b32 s56, s20, s44
	s_ashr_i32 s17, s16, 31
	s_lshl_b64 s[22:23], s[16:17], 19
	s_add_u32 s22, s3, s22
	s_addc_u32 s23, s30, s23
	s_and_b64 s[28:29], s[4:5], exec
	s_cselect_b32 s17, s23, s43
	s_cselect_b32 s57, s22, s42
	s_add_u32 s58, s42, 0x10000
	s_addc_u32 s59, s43, 0
	s_add_u32 s42, s44, 0x40080
	v_mov_b32_e32 v2, 0
	s_addc_u32 s43, s45, 0
	s_mov_b32 s28, -2
	v_mov_b32_e32 v3, 0
	v_mov_b64_e32 v[4:5], 0
	v_mov_b64_e32 v[6:7], 0
	v_mov_b64_e32 v[8:9], 0
	v_mov_b64_e32 v[10:11], 0
	v_mov_b64_e32 v[12:13], 0
	v_mov_b64_e32 v[14:15], 0
	v_mov_b64_e32 v[16:17], 0
	v_mov_b64_e32 v[18:19], 0
	v_mov_b64_e32 v[20:21], 0
	v_mov_b64_e32 v[22:23], 0
	v_mov_b64_e32 v[24:25], 0
	v_mov_b64_e32 v[26:27], 0
	v_mov_b64_e32 v[28:29], 0
	v_mov_b64_e32 v[30:31], 0
	v_mov_b64_e32 v[32:33], 0
	v_mov_b64_e32 v[34:35], 0
	v_mov_b64_e32 v[36:37], 0
	v_mov_b64_e32 v[38:39], 0
	v_mov_b64_e32 v[40:41], 0
	v_mov_b64_e32 v[42:43], 0
	v_mov_b64_e32 v[44:45], 0
	v_mov_b64_e32 v[46:47], 0
	v_mov_b64_e32 v[48:49], 0
	v_mov_b64_e32 v[50:51], 0
	v_mov_b64_e32 v[52:53], 0
	v_mov_b64_e32 v[54:55], 0
	v_mov_b64_e32 v[56:57], 0
	v_mov_b64_e32 v[58:59], 0
	v_mov_b64_e32 v[60:61], 0
	v_mov_b64_e32 v[62:63], 0
	v_mov_b64_e32 v[64:65], 0
	v_mov_b64_e32 v[66:67], 0
	v_mov_b64_e32 v[68:69], 0
	v_mov_b64_e32 v[70:71], 0
	v_mov_b64_e32 v[72:73], 0
	v_mov_b64_e32 v[74:75], 0
	v_mov_b64_e32 v[76:77], 0
	v_mov_b64_e32 v[78:79], 0
	v_mov_b64_e32 v[80:81], 0
	v_mov_b64_e32 v[82:83], 0
	v_mov_b64_e32 v[84:85], 0
	v_mov_b64_e32 v[86:87], 0
	v_mov_b64_e32 v[88:89], 0
	v_mov_b64_e32 v[90:91], 0
	v_mov_b64_e32 v[92:93], 0
	v_mov_b64_e32 v[94:95], 0
	v_mov_b64_e32 v[96:97], 0
	v_mov_b64_e32 v[98:99], 0
	v_mov_b64_e32 v[100:101], 0
	v_mov_b64_e32 v[102:103], 0
	v_mov_b64_e32 v[104:105], 0
	v_mov_b64_e32 v[106:107], 0
	v_mov_b64_e32 v[108:109], 0
	v_mov_b64_e32 v[110:111], 0
	v_mov_b64_e32 v[112:113], 0
	v_mov_b64_e32 v[114:115], 0
	v_mov_b64_e32 v[116:117], 0
	v_mov_b64_e32 v[118:119], 0
	v_mov_b64_e32 v[120:121], 0
	v_mov_b64_e32 v[122:123], 0
	v_mov_b64_e32 v[124:125], 0
	v_mov_b64_e32 v[126:127], 0
	v_mov_b64_e32 v[128:129], 0

.LBB0_1099:
	v_mov_b32_e32 v2, 0
	s_mov_b32 s6, 0
	s_mov_b64 s[50:51], -1
	s_mov_b64 s[52:53], 0
	v_mov_b32_e32 v3, 0
	v_mov_b64_e32 v[4:5], 0
	v_mov_b64_e32 v[6:7], 0
	v_mov_b64_e32 v[8:9], 0
	v_mov_b64_e32 v[10:11], 0
	v_mov_b64_e32 v[12:13], 0
	v_mov_b64_e32 v[14:15], 0
	v_mov_b64_e32 v[16:17], 0
	v_mov_b64_e32 v[18:19], 0
	v_mov_b64_e32 v[20:21], 0
	v_mov_b64_e32 v[22:23], 0
	v_mov_b64_e32 v[24:25], 0
	v_mov_b64_e32 v[26:27], 0
	v_mov_b64_e32 v[28:29], 0
	v_mov_b64_e32 v[30:31], 0
	v_mov_b64_e32 v[32:33], 0
	v_mov_b64_e32 v[34:35], 0
	v_mov_b64_e32 v[36:37], 0
	v_mov_b64_e32 v[38:39], 0
	v_mov_b64_e32 v[40:41], 0
	v_mov_b64_e32 v[42:43], 0
	v_mov_b64_e32 v[44:45], 0
	v_mov_b64_e32 v[46:47], 0
	v_mov_b64_e32 v[48:49], 0
	v_mov_b64_e32 v[50:51], 0
	v_mov_b64_e32 v[52:53], 0
	v_mov_b64_e32 v[54:55], 0
	v_mov_b64_e32 v[56:57], 0
	v_mov_b64_e32 v[58:59], 0
	v_mov_b64_e32 v[60:61], 0
	v_mov_b64_e32 v[62:63], 0
	v_mov_b64_e32 v[64:65], 0
	v_mov_b64_e32 v[66:67], 0
	v_mov_b64_e32 v[68:69], 0
	v_mov_b64_e32 v[70:71], 0
	v_mov_b64_e32 v[72:73], 0
	v_mov_b64_e32 v[74:75], 0
	v_mov_b64_e32 v[76:77], 0
	v_mov_b64_e32 v[78:79], 0
	v_mov_b64_e32 v[80:81], 0
	v_mov_b64_e32 v[82:83], 0
	v_mov_b64_e32 v[84:85], 0
	v_mov_b64_e32 v[86:87], 0
	v_mov_b64_e32 v[88:89], 0
	v_mov_b64_e32 v[90:91], 0
	v_mov_b64_e32 v[92:93], 0
	v_mov_b64_e32 v[94:95], 0
	v_mov_b64_e32 v[96:97], 0
	v_mov_b64_e32 v[98:99], 0
	v_mov_b64_e32 v[100:101], 0
	v_mov_b64_e32 v[102:103], 0
	v_mov_b64_e32 v[104:105], 0
	v_mov_b64_e32 v[106:107], 0
	v_mov_b64_e32 v[108:109], 0
	v_mov_b64_e32 v[110:111], 0
	v_mov_b64_e32 v[112:113], 0
	v_mov_b64_e32 v[114:115], 0
	v_mov_b64_e32 v[116:117], 0
	v_mov_b64_e32 v[118:119], 0
	v_mov_b64_e32 v[120:121], 0
	v_mov_b64_e32 v[122:123], 0
	v_mov_b64_e32 v[124:125], 0
	v_mov_b64_e32 v[126:127], 0
	v_mov_b64_e32 v[128:129], 0

.LBB0_1266:
	s_cmp_lt_i32 s42, 0
	s_cselect_b32 s33, 16, 4
	s_add_i32 s43, s33, -2
	s_add_u32 s45, s56, 0x10000
	s_addc_u32 s47, s57, 0
	s_add_u32 s56, s58, 0x40080
	v_mov_b32_e32 v2, 0
	s_mov_b32 s28, 0
	s_addc_u32 s57, s59, 0
	v_mov_b32_e32 v3, 0
	v_mov_b64_e32 v[4:5], 0
	v_mov_b64_e32 v[6:7], 0
	v_mov_b64_e32 v[8:9], 0
	v_mov_b64_e32 v[10:11], 0
	v_mov_b64_e32 v[12:13], 0
	v_mov_b64_e32 v[14:15], 0
	v_mov_b64_e32 v[16:17], 0
	v_mov_b64_e32 v[18:19], 0
	v_mov_b64_e32 v[20:21], 0
	v_mov_b64_e32 v[22:23], 0
	v_mov_b64_e32 v[24:25], 0
	v_mov_b64_e32 v[26:27], 0
	v_mov_b64_e32 v[28:29], 0
	v_mov_b64_e32 v[30:31], 0
	v_mov_b64_e32 v[32:33], 0
	v_mov_b64_e32 v[34:35], 0
	v_mov_b64_e32 v[36:37], 0
	v_mov_b64_e32 v[38:39], 0
	v_mov_b64_e32 v[40:41], 0
	v_mov_b64_e32 v[42:43], 0
	v_mov_b64_e32 v[44:45], 0
	v_mov_b64_e32 v[46:47], 0
	v_mov_b64_e32 v[48:49], 0
	v_mov_b64_e32 v[50:51], 0
	v_mov_b64_e32 v[52:53], 0
	v_mov_b64_e32 v[54:55], 0
	v_mov_b64_e32 v[56:57], 0
	v_mov_b64_e32 v[58:59], 0
	v_mov_b64_e32 v[60:61], 0
	v_mov_b64_e32 v[62:63], 0
	v_mov_b64_e32 v[64:65], 0
	v_mov_b64_e32 v[66:67], 0
	v_mov_b64_e32 v[68:69], 0
	v_mov_b64_e32 v[70:71], 0
	v_mov_b64_e32 v[72:73], 0
	v_mov_b64_e32 v[74:75], 0
	v_mov_b64_e32 v[76:77], 0
	v_mov_b64_e32 v[78:79], 0
	v_mov_b64_e32 v[80:81], 0
	v_mov_b64_e32 v[82:83], 0
	v_mov_b64_e32 v[84:85], 0
	v_mov_b64_e32 v[86:87], 0
	v_mov_b64_e32 v[88:89], 0
	v_mov_b64_e32 v[90:91], 0
	v_mov_b64_e32 v[92:93], 0
	v_mov_b64_e32 v[94:95], 0
	v_mov_b64_e32 v[96:97], 0
	v_mov_b64_e32 v[98:99], 0
	v_mov_b64_e32 v[100:101], 0
	v_mov_b64_e32 v[102:103], 0
	v_mov_b64_e32 v[104:105], 0
	v_mov_b64_e32 v[106:107], 0
	v_mov_b64_e32 v[108:109], 0
	v_mov_b64_e32 v[110:111], 0
	v_mov_b64_e32 v[112:113], 0
	v_mov_b64_e32 v[114:115], 0
	v_mov_b64_e32 v[116:117], 0
	v_mov_b64_e32 v[118:119], 0
	v_mov_b64_e32 v[120:121], 0
	v_mov_b64_e32 v[122:123], 0
	v_mov_b64_e32 v[124:125], 0
	v_mov_b64_e32 v[126:127], 0
	v_mov_b64_e32 v[128:129], 0

.LBB0_1518:
	s_lshl_b32 s8, s88, 8
	v_add_u32_e32 v4, s8, v1
	v_add_u32_e32 v6, s8, v164
	s_bitset1_b32 s8, 7
	v_add_u32_e32 v8, s8, v1
	v_add_u32_e32 v10, s8, v164
	v_ashrrev_i32_e32 v5, 31, v4
	v_ashrrev_i32_e32 v7, 31, v6
	v_ashrrev_i32_e32 v9, 31, v8
	v_ashrrev_i32_e32 v11, 31, v10
	v_mov_b32_e32 v147, v135
	v_mov_b32_e32 v149, v135
	v_lshl_add_u64 v[158:159], v[2:3], 0, s[46:47]
	v_mov_b32_e32 v2, 0
	v_lshl_add_u64 v[150:151], v[4:5], 2, s[12:13]
	v_lshl_add_u64 v[152:153], v[6:7], 2, s[12:13]
	v_lshl_add_u64 v[154:155], v[8:9], 2, s[12:13]
	v_lshl_add_u64 v[156:157], v[10:11], 2, s[12:13]
	v_lshl_add_u64 v[160:161], s[20:21], 0, v[146:147]
	v_lshl_add_u64 v[162:163], s[20:21], 0, v[148:149]
	s_mov_b32 s51, -2
	s_mov_b64 s[54:55], 0
	v_mov_b32_e32 v147, v141
	v_mov_b32_e32 v149, v144
	v_mov_b32_e32 v169, v146
	v_mov_b32_e32 v171, v148
	v_mov_b32_e32 v3, 0
	v_mov_b64_e32 v[4:5], 0
	v_mov_b64_e32 v[6:7], 0
	v_mov_b64_e32 v[8:9], 0
	v_mov_b64_e32 v[10:11], 0
	v_mov_b64_e32 v[12:13], 0
	v_mov_b64_e32 v[14:15], 0
	v_mov_b64_e32 v[16:17], 0
	v_mov_b64_e32 v[18:19], 0
	v_mov_b64_e32 v[20:21], 0
	v_mov_b64_e32 v[22:23], 0
	v_mov_b64_e32 v[24:25], 0
	v_mov_b64_e32 v[26:27], 0
	v_mov_b64_e32 v[28:29], 0
	v_mov_b64_e32 v[30:31], 0
	v_mov_b64_e32 v[32:33], 0
	v_mov_b64_e32 v[34:35], 0
	v_mov_b64_e32 v[36:37], 0
	v_mov_b64_e32 v[38:39], 0
	v_mov_b64_e32 v[40:41], 0
	v_mov_b64_e32 v[42:43], 0
	v_mov_b64_e32 v[44:45], 0
	v_mov_b64_e32 v[46:47], 0
	v_mov_b64_e32 v[48:49], 0
	v_mov_b64_e32 v[50:51], 0
	v_mov_b64_e32 v[52:53], 0
	v_mov_b64_e32 v[54:55], 0
	v_mov_b64_e32 v[56:57], 0
	v_mov_b64_e32 v[58:59], 0
	v_mov_b64_e32 v[60:61], 0
	v_mov_b64_e32 v[62:63], 0
	v_mov_b64_e32 v[64:65], 0
	v_mov_b64_e32 v[66:67], 0
	v_mov_b64_e32 v[68:69], 0
	v_mov_b64_e32 v[70:71], 0
	v_mov_b64_e32 v[72:73], 0
	v_mov_b64_e32 v[74:75], 0
	v_mov_b64_e32 v[76:77], 0
	v_mov_b64_e32 v[78:79], 0
	v_mov_b64_e32 v[80:81], 0
	v_mov_b64_e32 v[82:83], 0
	v_mov_b64_e32 v[84:85], 0
	v_mov_b64_e32 v[86:87], 0
	v_mov_b64_e32 v[88:89], 0
	v_mov_b64_e32 v[90:91], 0
	v_mov_b64_e32 v[92:93], 0
	v_mov_b64_e32 v[94:95], 0
	v_mov_b64_e32 v[96:97], 0
	v_mov_b64_e32 v[98:99], 0
	v_mov_b64_e32 v[100:101], 0
	v_mov_b64_e32 v[102:103], 0
	v_mov_b64_e32 v[104:105], 0
	v_mov_b64_e32 v[106:107], 0
	v_mov_b64_e32 v[108:109], 0
	v_mov_b64_e32 v[110:111], 0
	v_mov_b64_e32 v[112:113], 0
	v_mov_b64_e32 v[114:115], 0
	v_mov_b64_e32 v[116:117], 0
	v_mov_b64_e32 v[118:119], 0
	v_mov_b64_e32 v[120:121], 0
	v_mov_b64_e32 v[122:123], 0
	v_mov_b64_e32 v[124:125], 0
	v_mov_b64_e32 v[126:127], 0
	v_mov_b64_e32 v[128:129], 0

.LBB0_1615:
	s_cmp_lt_i32 s6, 0
	s_cselect_b32 s28, 56, 14
	s_add_i32 s29, s28, -2
	s_add_u32 s62, s62, 0xc000
	v_lshl_add_u64 v[130:131], v[2:3], 0, s[48:49]
	v_mov_b32_e32 v2, 0
	s_mov_b32 s64, 0
	s_addc_u32 s63, s63, 0
	v_mov_b32_e32 v3, 0
	v_mov_b64_e32 v[4:5], 0
	v_mov_b64_e32 v[6:7], 0
	v_mov_b64_e32 v[8:9], 0
	v_mov_b64_e32 v[10:11], 0
	v_mov_b64_e32 v[12:13], 0
	v_mov_b64_e32 v[14:15], 0
	v_mov_b64_e32 v[16:17], 0
	v_mov_b64_e32 v[18:19], 0
	v_mov_b64_e32 v[20:21], 0
	v_mov_b64_e32 v[22:23], 0
	v_mov_b64_e32 v[24:25], 0
	v_mov_b64_e32 v[26:27], 0
	v_mov_b64_e32 v[28:29], 0
	v_mov_b64_e32 v[30:31], 0
	v_mov_b64_e32 v[32:33], 0
	v_mov_b64_e32 v[34:35], 0
	v_mov_b64_e32 v[36:37], 0
	v_mov_b64_e32 v[38:39], 0
	v_mov_b64_e32 v[40:41], 0
	v_mov_b64_e32 v[42:43], 0
	v_mov_b64_e32 v[44:45], 0
	v_mov_b64_e32 v[46:47], 0
	v_mov_b64_e32 v[48:49], 0
	v_mov_b64_e32 v[50:51], 0
	v_mov_b64_e32 v[52:53], 0
	v_mov_b64_e32 v[54:55], 0
	v_mov_b64_e32 v[56:57], 0
	v_mov_b64_e32 v[58:59], 0
	v_mov_b64_e32 v[60:61], 0
	v_mov_b64_e32 v[62:63], 0
	v_mov_b64_e32 v[64:65], 0
	v_mov_b64_e32 v[66:67], 0
	v_mov_b64_e32 v[68:69], 0
	v_mov_b64_e32 v[70:71], 0
	v_mov_b64_e32 v[72:73], 0
	v_mov_b64_e32 v[74:75], 0
	v_mov_b64_e32 v[76:77], 0
	v_mov_b64_e32 v[78:79], 0
	v_mov_b64_e32 v[80:81], 0
	v_mov_b64_e32 v[82:83], 0
	v_mov_b64_e32 v[84:85], 0
	v_mov_b64_e32 v[86:87], 0
	v_mov_b64_e32 v[88:89], 0
	v_mov_b64_e32 v[90:91], 0
	v_mov_b64_e32 v[92:93], 0
	v_mov_b64_e32 v[94:95], 0
	v_mov_b64_e32 v[96:97], 0
	v_mov_b64_e32 v[98:99], 0
	v_mov_b64_e32 v[100:101], 0
	v_mov_b64_e32 v[102:103], 0
	v_mov_b64_e32 v[104:105], 0
	v_mov_b64_e32 v[106:107], 0
	v_mov_b64_e32 v[108:109], 0
	v_mov_b64_e32 v[110:111], 0
	v_mov_b64_e32 v[112:113], 0
	v_mov_b64_e32 v[114:115], 0
	v_mov_b64_e32 v[116:117], 0
	v_mov_b64_e32 v[118:119], 0
	v_mov_b64_e32 v[120:121], 0
	v_mov_b64_e32 v[122:123], 0
	v_mov_b64_e32 v[124:125], 0
	v_mov_b64_e32 v[126:127], 0
	v_mov_b64_e32 v[128:129], 0

.LBB0_1948:
	s_cmp_lt_i32 s40, 0
	s_cselect_b32 s41, 48, 4
	s_add_i32 s73, s41, -2
	s_add_u32 s75, s48, 0x10000
	v_mov_b32_e32 v2, 0
	s_mov_b32 s29, 0
	s_addc_u32 s28, s49, 0
	v_mov_b32_e32 v3, 0
	v_mov_b64_e32 v[4:5], 0
	v_mov_b64_e32 v[6:7], 0
	v_mov_b64_e32 v[8:9], 0
	v_mov_b64_e32 v[10:11], 0
	v_mov_b64_e32 v[12:13], 0
	v_mov_b64_e32 v[14:15], 0
	v_mov_b64_e32 v[16:17], 0
	v_mov_b64_e32 v[18:19], 0
	v_mov_b64_e32 v[20:21], 0
	v_mov_b64_e32 v[22:23], 0
	v_mov_b64_e32 v[24:25], 0
	v_mov_b64_e32 v[26:27], 0
	v_mov_b64_e32 v[28:29], 0
	v_mov_b64_e32 v[30:31], 0
	v_mov_b64_e32 v[32:33], 0
	v_mov_b64_e32 v[34:35], 0
	v_mov_b64_e32 v[36:37], 0
	v_mov_b64_e32 v[38:39], 0
	v_mov_b64_e32 v[40:41], 0
	v_mov_b64_e32 v[42:43], 0
	v_mov_b64_e32 v[44:45], 0
	v_mov_b64_e32 v[46:47], 0
	v_mov_b64_e32 v[48:49], 0
	v_mov_b64_e32 v[50:51], 0
	v_mov_b64_e32 v[52:53], 0
	v_mov_b64_e32 v[54:55], 0
	v_mov_b64_e32 v[56:57], 0
	v_mov_b64_e32 v[58:59], 0
	v_mov_b64_e32 v[60:61], 0
	v_mov_b64_e32 v[62:63], 0
	v_mov_b64_e32 v[64:65], 0
	v_mov_b64_e32 v[66:67], 0
	v_mov_b64_e32 v[68:69], 0
	v_mov_b64_e32 v[70:71], 0
	v_mov_b64_e32 v[72:73], 0
	v_mov_b64_e32 v[74:75], 0
	v_mov_b64_e32 v[76:77], 0
	v_mov_b64_e32 v[78:79], 0
	v_mov_b64_e32 v[80:81], 0
	v_mov_b64_e32 v[82:83], 0
	v_mov_b64_e32 v[84:85], 0
	v_mov_b64_e32 v[86:87], 0
	v_mov_b64_e32 v[88:89], 0
	v_mov_b64_e32 v[90:91], 0
	v_mov_b64_e32 v[92:93], 0
	v_mov_b64_e32 v[94:95], 0
	v_mov_b64_e32 v[96:97], 0
	v_mov_b64_e32 v[98:99], 0
	v_mov_b64_e32 v[100:101], 0
	v_mov_b64_e32 v[102:103], 0
	v_mov_b64_e32 v[104:105], 0
	v_mov_b64_e32 v[106:107], 0
	v_mov_b64_e32 v[108:109], 0
	v_mov_b64_e32 v[110:111], 0
	v_mov_b64_e32 v[112:113], 0
	v_mov_b64_e32 v[114:115], 0
	v_mov_b64_e32 v[116:117], 0
	v_mov_b64_e32 v[118:119], 0
	v_mov_b64_e32 v[120:121], 0
	v_mov_b64_e32 v[122:123], 0
	v_mov_b64_e32 v[124:125], 0
	v_mov_b64_e32 v[126:127], 0
	v_mov_b64_e32 v[128:129], 0

.LBB0_2078:
	s_ashr_i32 s17, s16, 31
	s_lshl_b64 s[18:19], s[16:17], 19
	s_add_u32 s18, s38, s18
	s_addc_u32 s19, s39, s19
	s_and_b64 s[20:21], s[4:5], exec
	s_cselect_b32 s17, s19, s45
	s_cselect_b32 s41, s18, s44
	s_ashr_i32 s15, s14, 31
	s_lshl_b64 s[20:21], s[14:15], 19
	s_add_u32 s20, s3, s20
	s_addc_u32 s21, s30, s21
	s_and_b64 s[28:29], s[4:5], exec
	s_cselect_b32 s15, s21, s43
	s_cselect_b32 s62, s20, s42
	s_add_u32 s63, s42, 0x10000
	s_addc_u32 s64, s43, 0
	s_add_u32 s42, s44, 0x40080
	v_mov_b32_e32 v2, 0
	s_addc_u32 s43, s45, 0
	s_mov_b32 s28, -2
	v_mov_b32_e32 v3, 0
	v_mov_b64_e32 v[4:5], 0
	v_mov_b64_e32 v[6:7], 0
	v_mov_b64_e32 v[8:9], 0
	v_mov_b64_e32 v[10:11], 0
	v_mov_b64_e32 v[12:13], 0
	v_mov_b64_e32 v[14:15], 0
	v_mov_b64_e32 v[16:17], 0
	v_mov_b64_e32 v[18:19], 0
	v_mov_b64_e32 v[20:21], 0
	v_mov_b64_e32 v[22:23], 0
	v_mov_b64_e32 v[24:25], 0
	v_mov_b64_e32 v[26:27], 0
	v_mov_b64_e32 v[28:29], 0
	v_mov_b64_e32 v[30:31], 0
	v_mov_b64_e32 v[32:33], 0
	v_mov_b64_e32 v[34:35], 0
	v_mov_b64_e32 v[36:37], 0
	v_mov_b64_e32 v[38:39], 0
	v_mov_b64_e32 v[40:41], 0
	v_mov_b64_e32 v[42:43], 0
	v_mov_b64_e32 v[44:45], 0
	v_mov_b64_e32 v[46:47], 0
	v_mov_b64_e32 v[48:49], 0
	v_mov_b64_e32 v[50:51], 0
	v_mov_b64_e32 v[52:53], 0
	v_mov_b64_e32 v[54:55], 0
	v_mov_b64_e32 v[56:57], 0
	v_mov_b64_e32 v[58:59], 0
	v_mov_b64_e32 v[60:61], 0
	v_mov_b64_e32 v[62:63], 0
	v_mov_b64_e32 v[64:65], 0
	v_mov_b64_e32 v[66:67], 0
	v_mov_b64_e32 v[68:69], 0
	v_mov_b64_e32 v[70:71], 0
	v_mov_b64_e32 v[72:73], 0
	v_mov_b64_e32 v[74:75], 0
	v_mov_b64_e32 v[76:77], 0
	v_mov_b64_e32 v[78:79], 0
	v_mov_b64_e32 v[80:81], 0
	v_mov_b64_e32 v[82:83], 0
	v_mov_b64_e32 v[84:85], 0
	v_mov_b64_e32 v[86:87], 0
	v_mov_b64_e32 v[88:89], 0
	v_mov_b64_e32 v[90:91], 0
	v_mov_b64_e32 v[92:93], 0
	v_mov_b64_e32 v[94:95], 0
	v_mov_b64_e32 v[96:97], 0
	v_mov_b64_e32 v[98:99], 0
	v_mov_b64_e32 v[100:101], 0
	v_mov_b64_e32 v[102:103], 0
	v_mov_b64_e32 v[104:105], 0
	v_mov_b64_e32 v[106:107], 0
	v_mov_b64_e32 v[108:109], 0
	v_mov_b64_e32 v[110:111], 0
	v_mov_b64_e32 v[112:113], 0
	v_mov_b64_e32 v[114:115], 0
	v_mov_b64_e32 v[116:117], 0
	v_mov_b64_e32 v[118:119], 0
	v_mov_b64_e32 v[120:121], 0
	v_mov_b64_e32 v[122:123], 0
	v_mov_b64_e32 v[124:125], 0
	v_mov_b64_e32 v[126:127], 0
	v_mov_b64_e32 v[128:129], 0

.LBB0_2163:
	s_cmp_lt_i32 s22, 0
	s_cselect_b32 s23, 44, 4
	s_add_i32 s73, s23, -2
	s_add_u32 s44, s44, 0xc000
	s_addc_u32 s45, s45, 0
	s_add_u32 s75, s46, 0x10000
	v_mov_b32_e32 v2, 0
	s_mov_b32 s28, 0
	s_addc_u32 s76, s47, 0
	v_mov_b32_e32 v3, 0
	v_mov_b64_e32 v[4:5], 0
	v_mov_b64_e32 v[6:7], 0
	v_mov_b64_e32 v[8:9], 0
	v_mov_b64_e32 v[10:11], 0
	v_mov_b64_e32 v[12:13], 0
	v_mov_b64_e32 v[14:15], 0
	v_mov_b64_e32 v[16:17], 0
	v_mov_b64_e32 v[18:19], 0
	v_mov_b64_e32 v[20:21], 0
	v_mov_b64_e32 v[22:23], 0
	v_mov_b64_e32 v[24:25], 0
	v_mov_b64_e32 v[26:27], 0
	v_mov_b64_e32 v[28:29], 0
	v_mov_b64_e32 v[30:31], 0
	v_mov_b64_e32 v[32:33], 0
	v_mov_b64_e32 v[34:35], 0
	v_mov_b64_e32 v[36:37], 0
	v_mov_b64_e32 v[38:39], 0
	v_mov_b64_e32 v[40:41], 0
	v_mov_b64_e32 v[42:43], 0
	v_mov_b64_e32 v[44:45], 0
	v_mov_b64_e32 v[46:47], 0
	v_mov_b64_e32 v[48:49], 0
	v_mov_b64_e32 v[50:51], 0
	v_mov_b64_e32 v[52:53], 0
	v_mov_b64_e32 v[54:55], 0
	v_mov_b64_e32 v[56:57], 0
	v_mov_b64_e32 v[58:59], 0
	v_mov_b64_e32 v[60:61], 0
	v_mov_b64_e32 v[62:63], 0
	v_mov_b64_e32 v[64:65], 0
	v_mov_b64_e32 v[66:67], 0
	v_mov_b64_e32 v[68:69], 0
	v_mov_b64_e32 v[70:71], 0
	v_mov_b64_e32 v[72:73], 0
	v_mov_b64_e32 v[74:75], 0
	v_mov_b64_e32 v[76:77], 0
	v_mov_b64_e32 v[78:79], 0
	v_mov_b64_e32 v[80:81], 0
	v_mov_b64_e32 v[82:83], 0
	v_mov_b64_e32 v[84:85], 0
	v_mov_b64_e32 v[86:87], 0
	v_mov_b64_e32 v[88:89], 0
	v_mov_b64_e32 v[90:91], 0
	v_mov_b64_e32 v[92:93], 0
	v_mov_b64_e32 v[94:95], 0
	v_mov_b64_e32 v[96:97], 0
	v_mov_b64_e32 v[98:99], 0
	v_mov_b64_e32 v[100:101], 0
	v_mov_b64_e32 v[102:103], 0
	v_mov_b64_e32 v[104:105], 0
	v_mov_b64_e32 v[106:107], 0
	v_mov_b64_e32 v[108:109], 0
	v_mov_b64_e32 v[110:111], 0
	v_mov_b64_e32 v[112:113], 0
	v_mov_b64_e32 v[114:115], 0
	v_mov_b64_e32 v[116:117], 0
	v_mov_b64_e32 v[118:119], 0
	v_mov_b64_e32 v[120:121], 0
	v_mov_b64_e32 v[122:123], 0
	v_mov_b64_e32 v[124:125], 0
	v_mov_b64_e32 v[126:127], 0
	v_mov_b64_e32 v[128:129], 0

.LBB0_2293:
	s_ashr_i32 s15, s14, 31
	s_lshl_b64 s[16:17], s[14:15], 19
	s_add_u32 s16, s38, s16
	s_addc_u32 s17, s39, s17
	s_and_b64 s[18:19], s[4:5], exec
	s_cselect_b32 s15, s17, s41
	s_cselect_b32 s57, s16, s40
	s_ashr_i32 s13, s12, 31
	s_lshl_b64 s[18:19], s[12:13], 19
	s_add_u32 s18, s3, s18
	s_addc_u32 s19, s30, s19
	s_and_b64 s[28:29], s[4:5], exec
	s_cselect_b32 s13, s19, s23
	s_cselect_b32 s58, s18, s22
	s_add_u32 s59, s22, 0x10000
	s_addc_u32 s60, s23, 0
	s_add_u32 s22, s40, 0x40080
	v_mov_b32_e32 v2, 0
	s_addc_u32 s23, s41, 0
	s_mov_b32 s28, -2
	v_mov_b32_e32 v3, 0
	v_mov_b64_e32 v[4:5], 0
	v_mov_b64_e32 v[6:7], 0
	v_mov_b64_e32 v[8:9], 0
	v_mov_b64_e32 v[10:11], 0
	v_mov_b64_e32 v[12:13], 0
	v_mov_b64_e32 v[14:15], 0
	v_mov_b64_e32 v[16:17], 0
	v_mov_b64_e32 v[18:19], 0
	v_mov_b64_e32 v[20:21], 0
	v_mov_b64_e32 v[22:23], 0
	v_mov_b64_e32 v[24:25], 0
	v_mov_b64_e32 v[26:27], 0
	v_mov_b64_e32 v[28:29], 0
	v_mov_b64_e32 v[30:31], 0
	v_mov_b64_e32 v[32:33], 0
	v_mov_b64_e32 v[34:35], 0
	v_mov_b64_e32 v[36:37], 0
	v_mov_b64_e32 v[38:39], 0
	v_mov_b64_e32 v[40:41], 0
	v_mov_b64_e32 v[42:43], 0
	v_mov_b64_e32 v[44:45], 0
	v_mov_b64_e32 v[46:47], 0
	v_mov_b64_e32 v[48:49], 0
	v_mov_b64_e32 v[50:51], 0
	v_mov_b64_e32 v[52:53], 0
	v_mov_b64_e32 v[54:55], 0
	v_mov_b64_e32 v[56:57], 0
	v_mov_b64_e32 v[58:59], 0
	v_mov_b64_e32 v[60:61], 0
	v_mov_b64_e32 v[62:63], 0
	v_mov_b64_e32 v[64:65], 0
	v_mov_b64_e32 v[66:67], 0
	v_mov_b64_e32 v[68:69], 0
	v_mov_b64_e32 v[70:71], 0
	v_mov_b64_e32 v[72:73], 0
	v_mov_b64_e32 v[74:75], 0
	v_mov_b64_e32 v[76:77], 0
	v_mov_b64_e32 v[78:79], 0
	v_mov_b64_e32 v[80:81], 0
	v_mov_b64_e32 v[82:83], 0
	v_mov_b64_e32 v[84:85], 0
	v_mov_b64_e32 v[86:87], 0
	v_mov_b64_e32 v[88:89], 0
	v_mov_b64_e32 v[90:91], 0
	v_mov_b64_e32 v[92:93], 0
	v_mov_b64_e32 v[94:95], 0
	v_mov_b64_e32 v[96:97], 0
	v_mov_b64_e32 v[98:99], 0
	v_mov_b64_e32 v[100:101], 0
	v_mov_b64_e32 v[102:103], 0
	v_mov_b64_e32 v[104:105], 0
	v_mov_b64_e32 v[106:107], 0
	v_mov_b64_e32 v[108:109], 0
	v_mov_b64_e32 v[110:111], 0
	v_mov_b64_e32 v[112:113], 0
	v_mov_b64_e32 v[114:115], 0
	v_mov_b64_e32 v[116:117], 0
	v_mov_b64_e32 v[118:119], 0
	v_mov_b64_e32 v[120:121], 0
	v_mov_b64_e32 v[122:123], 0
	v_mov_b64_e32 v[124:125], 0
	v_mov_b64_e32 v[126:127], 0
	v_mov_b64_e32 v[128:129], 0

.LBB0_2658:
	s_ashr_i32 s41, s40, 31
	s_lshl_b64 s[28:29], s[40:41], 20
	s_add_u32 s42, s30, s28
	s_addc_u32 s43, s31, s29
	s_and_b64 s[28:29], s[4:5], exec
	s_cselect_b32 s41, s43, s51
	s_cselect_b32 s70, s42, s50
	s_ashr_i32 s23, s22, 31
	s_lshl_b64 s[28:29], s[22:23], 20
	s_add_u32 s44, s36, s28
	s_addc_u32 s45, s37, s29
	s_and_b64 s[28:29], s[4:5], exec
	s_cselect_b32 s23, s45, s49
	s_cselect_b32 s71, s44, s48
	s_add_u32 s72, s48, 0x10000
	s_addc_u32 s73, s49, 0
	s_add_u32 s48, s50, 0x80080
	v_mov_b32_e32 v2, 0
	s_addc_u32 s49, s51, 0
	s_mov_b32 s28, -2
	v_mov_b32_e32 v3, 0
	v_mov_b64_e32 v[4:5], 0
	v_mov_b64_e32 v[6:7], 0
	v_mov_b64_e32 v[8:9], 0
	v_mov_b64_e32 v[10:11], 0
	v_mov_b64_e32 v[12:13], 0
	v_mov_b64_e32 v[14:15], 0
	v_mov_b64_e32 v[16:17], 0
	v_mov_b64_e32 v[18:19], 0
	v_mov_b64_e32 v[20:21], 0
	v_mov_b64_e32 v[22:23], 0
	v_mov_b64_e32 v[24:25], 0
	v_mov_b64_e32 v[26:27], 0
	v_mov_b64_e32 v[28:29], 0
	v_mov_b64_e32 v[30:31], 0
	v_mov_b64_e32 v[32:33], 0
	v_mov_b64_e32 v[34:35], 0
	v_mov_b64_e32 v[36:37], 0
	v_mov_b64_e32 v[38:39], 0
	v_mov_b64_e32 v[40:41], 0
	v_mov_b64_e32 v[42:43], 0
	v_mov_b64_e32 v[44:45], 0
	v_mov_b64_e32 v[46:47], 0
	v_mov_b64_e32 v[48:49], 0
	v_mov_b64_e32 v[50:51], 0
	v_mov_b64_e32 v[52:53], 0
	v_mov_b64_e32 v[54:55], 0
	v_mov_b64_e32 v[56:57], 0
	v_mov_b64_e32 v[58:59], 0
	v_mov_b64_e32 v[60:61], 0
	v_mov_b64_e32 v[62:63], 0
	v_mov_b64_e32 v[64:65], 0
	v_mov_b64_e32 v[66:67], 0
	v_mov_b64_e32 v[68:69], 0
	v_mov_b64_e32 v[70:71], 0
	v_mov_b64_e32 v[72:73], 0
	v_mov_b64_e32 v[74:75], 0
	v_mov_b64_e32 v[76:77], 0
	v_mov_b64_e32 v[78:79], 0
	v_mov_b64_e32 v[80:81], 0
	v_mov_b64_e32 v[82:83], 0
	v_mov_b64_e32 v[84:85], 0
	v_mov_b64_e32 v[86:87], 0
	v_mov_b64_e32 v[88:89], 0
	v_mov_b64_e32 v[90:91], 0
	v_mov_b64_e32 v[92:93], 0
	v_mov_b64_e32 v[94:95], 0
	v_mov_b64_e32 v[96:97], 0
	v_mov_b64_e32 v[98:99], 0
	v_mov_b64_e32 v[100:101], 0
	v_mov_b64_e32 v[102:103], 0
	v_mov_b64_e32 v[104:105], 0
	v_mov_b64_e32 v[106:107], 0
	v_mov_b64_e32 v[108:109], 0
	v_mov_b64_e32 v[110:111], 0
	v_mov_b64_e32 v[112:113], 0
	v_mov_b64_e32 v[114:115], 0
	v_mov_b64_e32 v[116:117], 0
	v_mov_b64_e32 v[118:119], 0
	v_mov_b64_e32 v[120:121], 0
	v_mov_b64_e32 v[138:139], 0
	v_mov_b64_e32 v[140:141], 0
	v_mov_b64_e32 v[142:143], 0
	v_mov_b64_e32 v[144:145], 0

.LBB0_2901:
	s_lshl_b32 s8, s86, 8
	v_add_u32_e32 v4, s8, v1
	v_add_u32_e32 v6, s8, v164
	s_bitset1_b32 s8, 7
	v_add_u32_e32 v8, s8, v1
	v_add_u32_e32 v10, s8, v164
	v_ashrrev_i32_e32 v5, 31, v4
	v_ashrrev_i32_e32 v7, 31, v6
	v_ashrrev_i32_e32 v9, 31, v8
	v_ashrrev_i32_e32 v11, 31, v10
	v_mov_b32_e32 v147, v135
	v_mov_b32_e32 v149, v135
	v_lshl_add_u64 v[158:159], v[2:3], 0, s[44:45]
	v_mov_b32_e32 v2, 0
	v_lshl_add_u64 v[150:151], v[4:5], 2, s[12:13]
	v_lshl_add_u64 v[152:153], v[6:7], 2, s[12:13]
	v_lshl_add_u64 v[154:155], v[8:9], 2, s[12:13]
	v_lshl_add_u64 v[156:157], v[10:11], 2, s[12:13]
	v_lshl_add_u64 v[160:161], s[20:21], 0, v[146:147]
	v_lshl_add_u64 v[162:163], s[20:21], 0, v[148:149]
	s_mov_b32 s49, -2
	s_mov_b64 s[52:53], 0
	v_mov_b32_e32 v147, v141
	v_mov_b32_e32 v149, v144
	v_mov_b32_e32 v169, v146
	v_mov_b32_e32 v171, v148
	v_mov_b32_e32 v3, 0
	v_mov_b64_e32 v[4:5], 0
	v_mov_b64_e32 v[6:7], 0
	v_mov_b64_e32 v[8:9], 0
	v_mov_b64_e32 v[10:11], 0
	v_mov_b64_e32 v[12:13], 0
	v_mov_b64_e32 v[14:15], 0
	v_mov_b64_e32 v[16:17], 0
	v_mov_b64_e32 v[18:19], 0
	v_mov_b64_e32 v[20:21], 0
	v_mov_b64_e32 v[22:23], 0
	v_mov_b64_e32 v[24:25], 0
	v_mov_b64_e32 v[26:27], 0
	v_mov_b64_e32 v[28:29], 0
	v_mov_b64_e32 v[30:31], 0
	v_mov_b64_e32 v[32:33], 0
	v_mov_b64_e32 v[34:35], 0
	v_mov_b64_e32 v[36:37], 0
	v_mov_b64_e32 v[38:39], 0
	v_mov_b64_e32 v[40:41], 0
	v_mov_b64_e32 v[42:43], 0
	v_mov_b64_e32 v[44:45], 0
	v_mov_b64_e32 v[46:47], 0
	v_mov_b64_e32 v[48:49], 0
	v_mov_b64_e32 v[50:51], 0
	v_mov_b64_e32 v[52:53], 0
	v_mov_b64_e32 v[54:55], 0
	v_mov_b64_e32 v[56:57], 0
	v_mov_b64_e32 v[58:59], 0
	v_mov_b64_e32 v[60:61], 0
	v_mov_b64_e32 v[62:63], 0
	v_mov_b64_e32 v[64:65], 0
	v_mov_b64_e32 v[66:67], 0
	v_mov_b64_e32 v[68:69], 0
	v_mov_b64_e32 v[70:71], 0
	v_mov_b64_e32 v[72:73], 0
	v_mov_b64_e32 v[74:75], 0
	v_mov_b64_e32 v[76:77], 0
	v_mov_b64_e32 v[78:79], 0
	v_mov_b64_e32 v[80:81], 0
	v_mov_b64_e32 v[82:83], 0
	v_mov_b64_e32 v[84:85], 0
	v_mov_b64_e32 v[86:87], 0
	v_mov_b64_e32 v[88:89], 0
	v_mov_b64_e32 v[90:91], 0
	v_mov_b64_e32 v[92:93], 0
	v_mov_b64_e32 v[94:95], 0
	v_mov_b64_e32 v[96:97], 0
	v_mov_b64_e32 v[98:99], 0
	v_mov_b64_e32 v[100:101], 0
	v_mov_b64_e32 v[102:103], 0
	v_mov_b64_e32 v[104:105], 0
	v_mov_b64_e32 v[106:107], 0
	v_mov_b64_e32 v[108:109], 0
	v_mov_b64_e32 v[110:111], 0
	v_mov_b64_e32 v[112:113], 0
	v_mov_b64_e32 v[114:115], 0
	v_mov_b64_e32 v[116:117], 0
	v_mov_b64_e32 v[118:119], 0
	v_mov_b64_e32 v[120:121], 0
	v_mov_b64_e32 v[122:123], 0
	v_mov_b64_e32 v[124:125], 0
	v_mov_b64_e32 v[126:127], 0
	v_mov_b64_e32 v[128:129], 0

.LBB0_2998:
	s_cmp_lt_i32 s6, 0
	s_cselect_b32 s28, 56, 14
	s_add_i32 s29, s28, -2
	s_add_u32 s58, s58, 0xc000
	v_lshl_add_u64 v[130:131], v[2:3], 0, s[44:45]
	v_mov_b32_e32 v2, 0
	s_mov_b32 s60, 0
	s_addc_u32 s59, s59, 0
	v_mov_b32_e32 v3, 0
	v_mov_b64_e32 v[4:5], 0
	v_mov_b64_e32 v[6:7], 0
	v_mov_b64_e32 v[8:9], 0
	v_mov_b64_e32 v[10:11], 0
	v_mov_b64_e32 v[12:13], 0
	v_mov_b64_e32 v[14:15], 0
	v_mov_b64_e32 v[16:17], 0
	v_mov_b64_e32 v[18:19], 0
	v_mov_b64_e32 v[20:21], 0
	v_mov_b64_e32 v[22:23], 0
	v_mov_b64_e32 v[24:25], 0
	v_mov_b64_e32 v[26:27], 0
	v_mov_b64_e32 v[28:29], 0
	v_mov_b64_e32 v[30:31], 0
	v_mov_b64_e32 v[32:33], 0
	v_mov_b64_e32 v[34:35], 0
	v_mov_b64_e32 v[36:37], 0
	v_mov_b64_e32 v[38:39], 0
	v_mov_b64_e32 v[40:41], 0
	v_mov_b64_e32 v[42:43], 0
	v_mov_b64_e32 v[44:45], 0
	v_mov_b64_e32 v[46:47], 0
	v_mov_b64_e32 v[48:49], 0
	v_mov_b64_e32 v[50:51], 0
	v_mov_b64_e32 v[52:53], 0
	v_mov_b64_e32 v[54:55], 0
	v_mov_b64_e32 v[56:57], 0
	v_mov_b64_e32 v[58:59], 0
	v_mov_b64_e32 v[60:61], 0
	v_mov_b64_e32 v[62:63], 0
	v_mov_b64_e32 v[64:65], 0
	v_mov_b64_e32 v[66:67], 0
	v_mov_b64_e32 v[68:69], 0
	v_mov_b64_e32 v[70:71], 0
	v_mov_b64_e32 v[72:73], 0
	v_mov_b64_e32 v[74:75], 0
	v_mov_b64_e32 v[76:77], 0
	v_mov_b64_e32 v[78:79], 0
	v_mov_b64_e32 v[80:81], 0
	v_mov_b64_e32 v[82:83], 0
	v_mov_b64_e32 v[84:85], 0
	v_mov_b64_e32 v[86:87], 0
	v_mov_b64_e32 v[88:89], 0
	v_mov_b64_e32 v[90:91], 0
	v_mov_b64_e32 v[92:93], 0
	v_mov_b64_e32 v[94:95], 0
	v_mov_b64_e32 v[96:97], 0
	v_mov_b64_e32 v[98:99], 0
	v_mov_b64_e32 v[100:101], 0
	v_mov_b64_e32 v[102:103], 0
	v_mov_b64_e32 v[104:105], 0
	v_mov_b64_e32 v[106:107], 0
	v_mov_b64_e32 v[108:109], 0
	v_mov_b64_e32 v[110:111], 0
	v_mov_b64_e32 v[112:113], 0
	v_mov_b64_e32 v[114:115], 0
	v_mov_b64_e32 v[116:117], 0
	v_mov_b64_e32 v[118:119], 0
	v_mov_b64_e32 v[120:121], 0
	v_mov_b64_e32 v[122:123], 0
	v_mov_b64_e32 v[124:125], 0
	v_mov_b64_e32 v[126:127], 0
	v_mov_b64_e32 v[128:129], 0
